# P11: loop-invariant final-norm gain loads hoisted out of the token loop (8 dwordx4 kept in v[200:231]); the three per-token vmcnt(0) round trips that also drained the result stores are gone
# speedup vs baseline: 1.0347x; 1.0037x over previous
.LBB0_1504:
	s_ashr_i32 s0, s4, 6
	v_readlane_b32 s1, v255, 16
	s_add_i32 s8, s0, s1
	s_cmpk_gt_i32 s8, 0x3fff
	s_cbranch_scc1 .LBB0_1507
	v_lshlrev_b32_e32 v1, 3, v0
	s_waitcnt vmcnt(0)
	v_and_b32_e32 v8, 0x1f8, v1
	v_mbcnt_lo_u32_b32 v1, -1, 0
	v_mbcnt_hi_u32_b32 v1, -1, v1
	v_and_b32_e32 v3, 64, v1
	v_add_u32_e32 v3, 64, v3
	v_xor_b32_e32 v4, 1, v1
	v_cmp_lt_i32_e32 vcc, v4, v3
	s_load_dwordx4 s[4:7], s[90:91], 0xf0
	s_add_u32 s10, s2, 0x44000000
	v_cndmask_b32_e32 v4, v1, v4, vcc
	v_lshlrev_b32_e32 v21, 2, v4
	v_xor_b32_e32 v4, 2, v1
	v_cmp_lt_i32_e32 vcc, v4, v3
	v_mov_b32_e32 v9, 0
	s_addc_u32 s11, s3, 0
	v_cndmask_b32_e32 v4, v1, v4, vcc
	v_lshlrev_b32_e32 v23, 2, v4
	v_xor_b32_e32 v4, 4, v1
	v_cmp_lt_i32_e32 vcc, v4, v3
	v_lshlrev_b32_e32 v2, 2, v8
	s_ashr_i32 s9, s8, 31
	v_cndmask_b32_e32 v4, v1, v4, vcc
	v_lshlrev_b32_e32 v25, 2, v4
	v_xor_b32_e32 v4, 8, v1
	v_cmp_lt_i32_e32 vcc, v4, v3
	v_mov_b32_e32 v5, v9
	s_lshl_b64 s[0:1], s[8:9], 12
	v_cndmask_b32_e32 v4, v1, v4, vcc
	v_lshlrev_b32_e32 v27, 2, v4
	v_xor_b32_e32 v4, 16, v1
	v_cmp_lt_i32_e32 vcc, v4, v3
	v_and_b32_e32 v0, 63, v0
	s_ashr_i32 s75, s74, 31
	v_cndmask_b32_e32 v4, v1, v4, vcc
	v_lshlrev_b32_e32 v28, 2, v4
	v_xor_b32_e32 v4, 32, v1
	v_cmp_lt_i32_e32 vcc, v4, v3
	v_mov_b32_e32 v3, v9
	s_waitcnt lgkmcnt(0)
	v_lshl_add_u64 v[10:11], s[4:5], 0, v[2:3]
	v_cndmask_b32_e32 v1, v1, v4, vcc
	v_or_b32_e32 v4, 0x1000, v2
	v_or_b32_e32 v2, 0x1800, v2
	v_lshl_add_u64 v[12:13], s[4:5], 0, v[4:5]
	v_lshl_add_u64 v[14:15], s[4:5], 0, v[2:3]
	v_lshl_or_b32 v16, v0, 4, s0
	v_mov_b32_e32 v17, s1
	s_lshl_b64 s[4:5], s[74:75], 12
	s_lshl_b64 s[0:1], s[8:9], 13
	s_add_u32 s0, s6, s0
	v_lshlrev_b32_e32 v29, 2, v1
	v_lshlrev_b32_e32 v0, 5, v0
	v_mov_b32_e32 v1, v9
	s_addc_u32 s1, s7, s1
	v_lshl_add_u64 v[0:1], s[0:1], 0, v[0:1]
	s_mov_b64 s[0:1], 0x1000
	v_lshl_add_u64 v[18:19], v[0:1], 0, s[0:1]
	s_lshl_b64 s[6:7], s[74:75], 13
	s_lshl_b64 s[12:13], s[8:9], 6
	s_lshl_b64 s[14:15], s[74:75], 6
	v_mov_b32_e32 v30, 0x5e30000
	s_add_i32 s9, 0, 0x21040
	v_mov_b32_e32 v31, 0x3727c5ac
	s_mov_b32 s16, 0xf800000
	v_mov_b32_e32 v32, 0x260
	global_load_dwordx4 v[200:203], v[10:11], off offset:16
	global_load_dwordx4 v[204:207], v[10:11], off
	global_load_dwordx4 v[208:211], v[10:11], off offset:2048
	global_load_dwordx4 v[212:215], v[10:11], off offset:2064
	global_load_dwordx4 v[216:219], v[12:13], off
	global_load_dwordx4 v[220:223], v[12:13], off offset:16
	global_load_dwordx4 v[224:227], v[14:15], off
	global_load_dwordx4 v[228:231], v[14:15], off offset:16
	s_waitcnt vmcnt(0)
.LBB0_1506:
	s_add_u32 s0, s2, s12
	s_addc_u32 s1, s3, s13
	v_mov_b32_e32 v0, v200
	v_mov_b32_e32 v1, v201
	v_mov_b32_e32 v2, v202
	v_mov_b32_e32 v3, v203
	v_mov_b32_e32 v4, v204
	v_mov_b32_e32 v5, v205
	v_mov_b32_e32 v6, v206
	v_mov_b32_e32 v7, v207
	global_load_dwordx3 v[50:52], v30, s[0:1]
	global_load_dwordx3 v[54:56], v30, s[0:1] offset:16
	global_load_dwordx3 v[58:60], v30, s[0:1] offset:32
	global_load_dwordx3 v[62:64], v30, s[0:1] offset:48
	v_lshl_add_u64 v[34:35], s[2:3], 0, v[16:17]
	v_add_co_u32_e32 v66, vcc, 0x22000000, v34
	s_add_i32 s8, s8, s74
	s_nop 0
	v_addc_co_u32_e32 v67, vcc, 0, v35, vcc
	global_load_dwordx4 v[34:37], v[66:67], off offset:3072
	global_load_dwordx4 v[38:41], v[66:67], off
	global_load_dwordx4 v[42:45], v[66:67], off offset:1024
	global_load_dwordx4 v[46:49], v[66:67], off offset:2048
	s_add_u32 s12, s12, s14
	s_addc_u32 s13, s13, s15
	v_lshl_add_u64 v[16:17], v[16:17], 0, s[4:5]
	s_cmpk_lt_i32 s8, 0x4000
	s_waitcnt vmcnt(7)
	v_lshlrev_b32_e32 v33, 2, v50
	s_waitcnt vmcnt(6)
	v_lshlrev_b32_e32 v57, 2, v54
	s_waitcnt vmcnt(5)
	v_lshlrev_b32_e32 v61, 2, v58
	s_waitcnt vmcnt(4)
	v_lshlrev_b32_e32 v62, 2, v62
	v_add_u32_e32 v33, s9, v33
	v_add_u32_e32 v75, s9, v57
	v_add_u32_e32 v77, s9, v61
	v_add_u32_e32 v79, s9, v62
	ds_read_b32 v74, v33
	ds_read_b32 v76, v75
	ds_read_b32 v78, v77
	ds_read_b32 v80, v79
	v_ashrrev_i32_e32 v67, 31, v51
	s_waitcnt lgkmcnt(3)
	v_ashrrev_i32_e32 v75, 31, v74
	s_waitcnt lgkmcnt(2)
	v_ashrrev_i32_e32 v77, 31, v76
	v_mov_b32_e32 v66, v51
	v_ashrrev_i32_e32 v51, 31, v55
	v_mov_b32_e32 v50, v55
	s_waitcnt lgkmcnt(1)
	v_ashrrev_i32_e32 v79, 31, v78
	s_waitcnt lgkmcnt(0)
	v_ashrrev_i32_e32 v81, 31, v80
	v_lshlrev_b64 v[74:75], 19, v[74:75]
	v_lshlrev_b64 v[76:77], 19, v[76:77]
	v_ashrrev_i32_e32 v55, 31, v59
	v_mov_b32_e32 v54, v59
	v_ashrrev_i32_e32 v59, 31, v63
	v_mov_b32_e32 v58, v63
	v_mov_b32_e32 v26, v52
	v_lshlrev_b64 v[52:53], 11, v[66:67]
	v_lshlrev_b64 v[50:51], 11, v[50:51]
	v_lshlrev_b64 v[78:79], 19, v[78:79]
	v_lshlrev_b64 v[80:81], 19, v[80:81]
	v_lshl_add_u64 v[74:75], s[10:11], 0, v[74:75]
	v_lshl_add_u64 v[76:77], s[10:11], 0, v[76:77]
	v_mov_b32_e32 v24, v56
	v_lshlrev_b64 v[54:55], 11, v[54:55]
	v_lshlrev_b64 v[56:57], 11, v[58:59]
	v_lshl_add_u64 v[78:79], s[10:11], 0, v[78:79]
	v_lshl_add_u64 v[80:81], s[10:11], 0, v[80:81]
	v_lshl_add_u64 v[52:53], v[74:75], 0, v[52:53]
	v_lshl_add_u64 v[50:51], v[76:77], 0, v[50:51]
	v_lshl_add_u64 v[54:55], v[78:79], 0, v[54:55]
	v_lshl_add_u64 v[56:57], v[80:81], 0, v[56:57]
	v_lshl_add_u64 v[52:53], v[52:53], 0, v[8:9]
	v_lshl_add_u64 v[50:51], v[50:51], 0, v[8:9]
	v_lshl_add_u64 v[54:55], v[54:55], 0, v[8:9]
	v_lshl_add_u64 v[56:57], v[56:57], 0, v[8:9]
	global_load_dwordx2 v[74:75], v[52:53], off
	global_load_dwordx2 v[76:77], v[52:53], off offset:512
	global_load_dwordx2 v[78:79], v[52:53], off offset:1024
	global_load_dwordx2 v[80:81], v[52:53], off offset:1536
	global_load_dwordx2 v[82:83], v[50:51], off
	global_load_dwordx2 v[84:85], v[50:51], off offset:512
	global_load_dwordx2 v[86:87], v[50:51], off offset:1024
	global_load_dwordx2 v[88:89], v[50:51], off offset:1536
	global_load_dwordx2 v[90:91], v[54:55], off
	global_load_dwordx2 v[92:93], v[54:55], off offset:512
	global_load_dwordx2 v[94:95], v[54:55], off offset:1024
	global_load_dwordx2 v[96:97], v[54:55], off offset:1536
	global_load_dwordx2 v[98:99], v[56:57], off
	global_load_dwordx2 v[100:101], v[56:57], off offset:512
	global_load_dwordx2 v[102:103], v[56:57], off offset:1024
	global_load_dwordx2 v[50:51], v[56:57], off offset:1536
	s_waitcnt vmcnt(18)
	v_cvt_f32_f16_e32 v62, v38
	v_cvt_f32_f16_sdwa v63, v38 dst_sel:DWORD dst_unused:UNUSED_PAD src0_sel:WORD_1
	v_cvt_f32_f16_e32 v38, v39
	v_cvt_f32_f16_sdwa v39, v39 dst_sel:DWORD dst_unused:UNUSED_PAD src0_sel:WORD_1
	v_mov_b32_e32 v22, v60
	v_mov_b32_e32 v20, v64
	v_cvt_f32_f16_e32 v58, v37
	v_cvt_f32_f16_sdwa v59, v37 dst_sel:DWORD dst_unused:UNUSED_PAD src0_sel:WORD_1
	v_cvt_f32_f16_e32 v60, v40
	v_cvt_f32_f16_sdwa v61, v40 dst_sel:DWORD dst_unused:UNUSED_PAD src0_sel:WORD_1
	v_cvt_f32_f16_e32 v40, v41
	v_cvt_f32_f16_sdwa v41, v41 dst_sel:DWORD dst_unused:UNUSED_PAD src0_sel:WORD_1
	s_waitcnt vmcnt(17)
	v_cvt_f32_f16_e32 v64, v44
	v_cvt_f32_f16_sdwa v65, v44 dst_sel:DWORD dst_unused:UNUSED_PAD src0_sel:WORD_1
	v_cvt_f32_f16_e32 v44, v45
	v_cvt_f32_f16_sdwa v45, v45 dst_sel:DWORD dst_unused:UNUSED_PAD src0_sel:WORD_1
	v_cvt_f32_f16_e32 v66, v42
	v_cvt_f32_f16_sdwa v67, v42 dst_sel:DWORD dst_unused:UNUSED_PAD src0_sel:WORD_1
	v_cvt_f32_f16_e32 v42, v43
	v_cvt_f32_f16_sdwa v43, v43 dst_sel:DWORD dst_unused:UNUSED_PAD src0_sel:WORD_1
	s_waitcnt vmcnt(16)
	v_cvt_f32_f16_e32 v68, v48
	v_cvt_f32_f16_sdwa v69, v48 dst_sel:DWORD dst_unused:UNUSED_PAD src0_sel:WORD_1
	v_cvt_f32_f16_e32 v48, v49
	v_cvt_f32_f16_sdwa v49, v49 dst_sel:DWORD dst_unused:UNUSED_PAD src0_sel:WORD_1
	v_cvt_f32_f16_e32 v70, v46
	v_cvt_f32_f16_sdwa v71, v46 dst_sel:DWORD dst_unused:UNUSED_PAD src0_sel:WORD_1
	v_cvt_f32_f16_e32 v46, v47
	v_cvt_f32_f16_sdwa v47, v47 dst_sel:DWORD dst_unused:UNUSED_PAD src0_sel:WORD_1
	v_cvt_f32_f16_e32 v72, v36
	v_cvt_f32_f16_sdwa v73, v36 dst_sel:DWORD dst_unused:UNUSED_PAD src0_sel:WORD_1
	v_cvt_f32_f16_e32 v36, v34
	v_cvt_f32_f16_sdwa v37, v34 dst_sel:DWORD dst_unused:UNUSED_PAD src0_sel:WORD_1
	v_cvt_f32_f16_e32 v34, v35
	v_cvt_f32_f16_sdwa v35, v35 dst_sel:DWORD dst_unused:UNUSED_PAD src0_sel:WORD_1
	s_waitcnt vmcnt(15)
	v_cvt_pk_f32_fp8_e32 v[52:53], v74
	v_cvt_pk_f32_fp8_sdwa v[54:55], v74 src0_sel:WORD_1
	v_cvt_pk_f32_fp8_e32 v[56:57], v75
	v_cvt_pk_f32_fp8_sdwa v[74:75], v75 src0_sel:WORD_1
	s_waitcnt vmcnt(11)
	v_cvt_pk_f32_fp8_e32 v[122:123], v82
	v_cvt_pk_f32_fp8_e32 v[104:105], v76
	v_cvt_pk_f32_fp8_sdwa v[106:107], v76 src0_sel:WORD_1
	v_cvt_pk_f32_fp8_e32 v[108:109], v77
	v_cvt_pk_f32_fp8_sdwa v[76:77], v77 src0_sel:WORD_1
	v_cvt_pk_f32_fp8_e32 v[110:111], v78
	v_cvt_pk_f32_fp8_sdwa v[112:113], v78 src0_sel:WORD_1
	v_cvt_pk_f32_fp8_e32 v[114:115], v79
	v_cvt_pk_f32_fp8_sdwa v[78:79], v79 src0_sel:WORD_1
	v_cvt_pk_f32_fp8_e32 v[116:117], v80
	v_cvt_pk_f32_fp8_sdwa v[118:119], v80 src0_sel:WORD_1
	v_cvt_pk_f32_fp8_e32 v[120:121], v81
	v_cvt_pk_f32_fp8_sdwa v[80:81], v81 src0_sel:WORD_1
	v_cvt_pk_f32_fp8_sdwa v[124:125], v82 src0_sel:WORD_1
	s_waitcnt vmcnt(7)
	v_cvt_pk_f32_fp8_e32 v[146:147], v90
	v_cvt_pk_f32_fp8_e32 v[126:127], v83
	v_cvt_pk_f32_fp8_sdwa v[82:83], v83 src0_sel:WORD_1
	v_cvt_pk_f32_fp8_e32 v[128:129], v84
	v_cvt_pk_f32_fp8_sdwa v[130:131], v84 src0_sel:WORD_1
	v_cvt_pk_f32_fp8_e32 v[132:133], v85
	v_cvt_pk_f32_fp8_sdwa v[84:85], v85 src0_sel:WORD_1
	v_cvt_pk_f32_fp8_e32 v[134:135], v86
	v_cvt_pk_f32_fp8_sdwa v[136:137], v86 src0_sel:WORD_1
	v_cvt_pk_f32_fp8_e32 v[138:139], v87
	v_cvt_pk_f32_fp8_sdwa v[86:87], v87 src0_sel:WORD_1
	v_cvt_pk_f32_fp8_e32 v[140:141], v88
	v_cvt_pk_f32_fp8_sdwa v[142:143], v88 src0_sel:WORD_1
	v_cvt_pk_f32_fp8_e32 v[144:145], v89
	v_cvt_pk_f32_fp8_sdwa v[88:89], v89 src0_sel:WORD_1
	v_cvt_pk_f32_fp8_sdwa v[148:149], v90 src0_sel:WORD_1
	s_waitcnt vmcnt(3)
	v_cvt_pk_f32_fp8_e32 v[170:171], v98
	v_cvt_pk_f32_fp8_e32 v[150:151], v91
	v_cvt_pk_f32_fp8_sdwa v[90:91], v91 src0_sel:WORD_1
	v_cvt_pk_f32_fp8_e32 v[152:153], v92
	v_cvt_pk_f32_fp8_sdwa v[154:155], v92 src0_sel:WORD_1
	v_cvt_pk_f32_fp8_e32 v[156:157], v93
	v_cvt_pk_f32_fp8_sdwa v[92:93], v93 src0_sel:WORD_1
	v_cvt_pk_f32_fp8_e32 v[158:159], v94
	v_cvt_pk_f32_fp8_sdwa v[160:161], v94 src0_sel:WORD_1
	v_cvt_pk_f32_fp8_e32 v[162:163], v95
	v_cvt_pk_f32_fp8_sdwa v[94:95], v95 src0_sel:WORD_1
	v_cvt_pk_f32_fp8_e32 v[164:165], v96
	v_cvt_pk_f32_fp8_sdwa v[166:167], v96 src0_sel:WORD_1
	v_cvt_pk_f32_fp8_e32 v[168:169], v97
	v_cvt_pk_f32_fp8_sdwa v[96:97], v97 src0_sel:WORD_1
	v_cvt_pk_f32_fp8_sdwa v[172:173], v98 src0_sel:WORD_1
	v_pk_fma_f32 v[52:53], v[26:27], v[52:53], v[62:63] op_sel_hi:[0,1,1]
	v_cvt_pk_f32_fp8_e32 v[174:175], v99
	v_cvt_pk_f32_fp8_sdwa v[98:99], v99 src0_sel:WORD_1
	s_waitcnt vmcnt(2)
	v_cvt_pk_f32_fp8_e32 v[176:177], v100
	v_cvt_pk_f32_fp8_sdwa v[178:179], v100 src0_sel:WORD_1
	v_cvt_pk_f32_fp8_e32 v[180:181], v101
	v_cvt_pk_f32_fp8_sdwa v[100:101], v101 src0_sel:WORD_1
	s_waitcnt vmcnt(1)
	v_cvt_pk_f32_fp8_e32 v[182:183], v102
	v_cvt_pk_f32_fp8_sdwa v[184:185], v102 src0_sel:WORD_1
	v_cvt_pk_f32_fp8_e32 v[186:187], v103
	v_cvt_pk_f32_fp8_sdwa v[102:103], v103 src0_sel:WORD_1
	s_waitcnt vmcnt(0)
	v_cvt_pk_f32_fp8_e32 v[188:189], v50
	v_cvt_pk_f32_fp8_sdwa v[190:191], v50 src0_sel:WORD_1
	v_cvt_pk_f32_fp8_e32 v[192:193], v51
	v_cvt_pk_f32_fp8_sdwa v[50:51], v51 src0_sel:WORD_1
	v_pk_fma_f32 v[38:39], v[26:27], v[54:55], v[38:39] op_sel_hi:[0,1,1]
	v_pk_fma_f32 v[52:53], v[24:25], v[122:123], v[52:53] op_sel_hi:[0,1,1]
	v_pk_fma_f32 v[58:59], v[26:27], v[80:81], v[58:59] op_sel_hi:[0,1,1]
	v_pk_fma_f32 v[56:57], v[26:27], v[56:57], v[60:61] op_sel_hi:[0,1,1]
	v_pk_fma_f32 v[40:41], v[26:27], v[74:75], v[40:41] op_sel_hi:[0,1,1]
	v_pk_fma_f32 v[54:55], v[26:27], v[108:109], v[64:65] op_sel_hi:[0,1,1]
	v_pk_fma_f32 v[44:45], v[26:27], v[76:77], v[44:45] op_sel_hi:[0,1,1]
	v_pk_fma_f32 v[60:61], v[26:27], v[104:105], v[66:67] op_sel_hi:[0,1,1]
	v_pk_fma_f32 v[42:43], v[26:27], v[106:107], v[42:43] op_sel_hi:[0,1,1]
	v_pk_fma_f32 v[62:63], v[26:27], v[114:115], v[68:69] op_sel_hi:[0,1,1]
	v_pk_fma_f32 v[48:49], v[26:27], v[78:79], v[48:49] op_sel_hi:[0,1,1]
	v_pk_fma_f32 v[64:65], v[26:27], v[110:111], v[70:71] op_sel_hi:[0,1,1]
	v_pk_fma_f32 v[46:47], v[26:27], v[112:113], v[46:47] op_sel_hi:[0,1,1]
	v_pk_fma_f32 v[66:67], v[26:27], v[120:121], v[72:73] op_sel_hi:[0,1,1]
	v_pk_fma_f32 v[36:37], v[26:27], v[116:117], v[36:37] op_sel_hi:[0,1,1]
	v_pk_fma_f32 v[34:35], v[26:27], v[118:119], v[34:35] op_sel_hi:[0,1,1]
	v_pk_fma_f32 v[38:39], v[24:25], v[124:125], v[38:39] op_sel_hi:[0,1,1]
	v_pk_fma_f32 v[52:53], v[22:23], v[146:147], v[52:53] op_sel_hi:[0,1,1]
	v_pk_fma_f32 v[58:59], v[24:25], v[88:89], v[58:59] op_sel_hi:[0,1,1]
	v_pk_fma_f32 v[56:57], v[24:25], v[126:127], v[56:57] op_sel_hi:[0,1,1]
	v_pk_fma_f32 v[40:41], v[24:25], v[82:83], v[40:41] op_sel_hi:[0,1,1]
	v_pk_fma_f32 v[54:55], v[24:25], v[132:133], v[54:55] op_sel_hi:[0,1,1]
	v_pk_fma_f32 v[44:45], v[24:25], v[84:85], v[44:45] op_sel_hi:[0,1,1]
	v_pk_fma_f32 v[60:61], v[24:25], v[128:129], v[60:61] op_sel_hi:[0,1,1]
	v_pk_fma_f32 v[42:43], v[24:25], v[130:131], v[42:43] op_sel_hi:[0,1,1]
	v_pk_fma_f32 v[62:63], v[24:25], v[138:139], v[62:63] op_sel_hi:[0,1,1]
	v_pk_fma_f32 v[48:49], v[24:25], v[86:87], v[48:49] op_sel_hi:[0,1,1]
	v_pk_fma_f32 v[64:65], v[24:25], v[134:135], v[64:65] op_sel_hi:[0,1,1]
	v_pk_fma_f32 v[46:47], v[24:25], v[136:137], v[46:47] op_sel_hi:[0,1,1]
	v_pk_fma_f32 v[66:67], v[24:25], v[144:145], v[66:67] op_sel_hi:[0,1,1]
	v_pk_fma_f32 v[36:37], v[24:25], v[140:141], v[36:37] op_sel_hi:[0,1,1]
	v_pk_fma_f32 v[34:35], v[24:25], v[142:143], v[34:35] op_sel_hi:[0,1,1]
	v_pk_fma_f32 v[38:39], v[22:23], v[148:149], v[38:39] op_sel_hi:[0,1,1]
	v_pk_fma_f32 v[52:53], v[20:21], v[170:171], v[52:53] op_sel_hi:[0,1,1]
	v_pk_fma_f32 v[58:59], v[22:23], v[96:97], v[58:59] op_sel_hi:[0,1,1]
	v_pk_fma_f32 v[56:57], v[22:23], v[150:151], v[56:57] op_sel_hi:[0,1,1]
	v_pk_fma_f32 v[40:41], v[22:23], v[90:91], v[40:41] op_sel_hi:[0,1,1]
	v_pk_fma_f32 v[54:55], v[22:23], v[156:157], v[54:55] op_sel_hi:[0,1,1]
	v_pk_fma_f32 v[44:45], v[22:23], v[92:93], v[44:45] op_sel_hi:[0,1,1]
	v_pk_fma_f32 v[60:61], v[22:23], v[152:153], v[60:61] op_sel_hi:[0,1,1]
	v_pk_fma_f32 v[42:43], v[22:23], v[154:155], v[42:43] op_sel_hi:[0,1,1]
	v_pk_fma_f32 v[62:63], v[22:23], v[162:163], v[62:63] op_sel_hi:[0,1,1]
	v_pk_fma_f32 v[48:49], v[22:23], v[94:95], v[48:49] op_sel_hi:[0,1,1]
	v_pk_fma_f32 v[64:65], v[22:23], v[158:159], v[64:65] op_sel_hi:[0,1,1]
	v_pk_fma_f32 v[46:47], v[22:23], v[160:161], v[46:47] op_sel_hi:[0,1,1]
	v_pk_fma_f32 v[66:67], v[22:23], v[168:169], v[66:67] op_sel_hi:[0,1,1]
	v_pk_fma_f32 v[36:37], v[22:23], v[164:165], v[36:37] op_sel_hi:[0,1,1]
	v_pk_fma_f32 v[34:35], v[22:23], v[166:167], v[34:35] op_sel_hi:[0,1,1]
	v_pk_fma_f32 v[38:39], v[20:21], v[172:173], v[38:39] op_sel_hi:[0,1,1]
	v_pk_mul_f32 v[72:73], v[52:53], v[52:53]
	v_pk_fma_f32 v[50:51], v[20:21], v[50:51], v[58:59] op_sel_hi:[0,1,1]
	v_pk_fma_f32 v[56:57], v[20:21], v[174:175], v[56:57] op_sel_hi:[0,1,1]
	v_pk_fma_f32 v[40:41], v[20:21], v[98:99], v[40:41] op_sel_hi:[0,1,1]
	v_pk_fma_f32 v[54:55], v[20:21], v[180:181], v[54:55] op_sel_hi:[0,1,1]
	v_pk_fma_f32 v[44:45], v[20:21], v[100:101], v[44:45] op_sel_hi:[0,1,1]
	v_pk_fma_f32 v[58:59], v[20:21], v[176:177], v[60:61] op_sel_hi:[0,1,1]
	v_pk_fma_f32 v[42:43], v[20:21], v[178:179], v[42:43] op_sel_hi:[0,1,1]
	v_pk_fma_f32 v[60:61], v[20:21], v[186:187], v[62:63] op_sel_hi:[0,1,1]
	v_pk_fma_f32 v[48:49], v[20:21], v[102:103], v[48:49] op_sel_hi:[0,1,1]
	v_pk_fma_f32 v[62:63], v[20:21], v[182:183], v[64:65] op_sel_hi:[0,1,1]
	v_pk_fma_f32 v[46:47], v[20:21], v[184:185], v[46:47] op_sel_hi:[0,1,1]
	v_pk_fma_f32 v[64:65], v[20:21], v[192:193], v[66:67] op_sel_hi:[0,1,1]
	v_pk_fma_f32 v[36:37], v[20:21], v[188:189], v[36:37] op_sel_hi:[0,1,1]
	v_pk_fma_f32 v[34:35], v[20:21], v[190:191], v[34:35] op_sel_hi:[0,1,1]
	v_pk_mul_f32 v[74:75], v[38:39], v[38:39]
	v_add_f32_e32 v20, v72, v73
	v_add_f32_e32 v20, v20, v74
	v_pk_mul_f32 v[68:69], v[56:57], v[56:57]
	v_add_f32_e32 v20, v75, v20
	v_add_f32_e32 v20, v68, v20
	v_pk_mul_f32 v[70:71], v[40:41], v[40:41]
	v_add_f32_e32 v20, v69, v20
	v_add_f32_e32 v20, v70, v20
	v_pk_mul_f32 v[80:81], v[58:59], v[58:59]
	v_add_f32_e32 v20, v71, v20
	v_add_f32_e32 v20, v80, v20
	v_pk_mul_f32 v[82:83], v[42:43], v[42:43]
	v_add_f32_e32 v20, v81, v20
	v_add_f32_e32 v20, v82, v20
	v_pk_mul_f32 v[76:77], v[54:55], v[54:55]
	v_add_f32_e32 v20, v83, v20
	v_add_f32_e32 v20, v76, v20
	v_pk_mul_f32 v[78:79], v[44:45], v[44:45]
	v_add_f32_e32 v20, v77, v20
	v_add_f32_e32 v20, v78, v20
	v_pk_mul_f32 v[88:89], v[62:63], v[62:63]
	v_add_f32_e32 v20, v79, v20
	v_add_f32_e32 v20, v88, v20
	v_pk_mul_f32 v[90:91], v[46:47], v[46:47]
	v_add_f32_e32 v20, v89, v20
	v_add_f32_e32 v20, v90, v20
	v_pk_mul_f32 v[84:85], v[60:61], v[60:61]
	v_add_f32_e32 v20, v91, v20
	v_add_f32_e32 v20, v84, v20
	v_pk_mul_f32 v[86:87], v[48:49], v[48:49]
	v_add_f32_e32 v20, v85, v20
	v_add_f32_e32 v20, v86, v20
	v_pk_mul_f32 v[94:95], v[36:37], v[36:37]
	v_add_f32_e32 v20, v87, v20
	v_add_f32_e32 v20, v94, v20
	v_pk_mul_f32 v[96:97], v[34:35], v[34:35]
	v_add_f32_e32 v20, v95, v20
	v_add_f32_e32 v20, v96, v20
	v_pk_mul_f32 v[92:93], v[64:65], v[64:65]
	v_add_f32_e32 v20, v97, v20
	v_add_f32_e32 v20, v92, v20
	v_pk_mul_f32 v[66:67], v[50:51], v[50:51]
	v_add_f32_e32 v20, v93, v20
	v_add_f32_e32 v20, v66, v20
	v_add_f32_e32 v20, v67, v20
	ds_bpermute_b32 v22, v21, v20
	s_waitcnt lgkmcnt(0)
	v_add_f32_e32 v20, v20, v22
	ds_bpermute_b32 v22, v23, v20
	s_waitcnt lgkmcnt(0)
	v_add_f32_e32 v20, v20, v22
	ds_bpermute_b32 v22, v25, v20
	s_waitcnt lgkmcnt(0)
	v_add_f32_e32 v20, v20, v22
	ds_bpermute_b32 v22, v27, v20
	s_waitcnt lgkmcnt(0)
	v_add_f32_e32 v20, v20, v22
	ds_bpermute_b32 v22, v28, v20
	s_waitcnt lgkmcnt(0)
	v_add_f32_e32 v20, v20, v22
	ds_bpermute_b32 v22, v29, v20
	s_waitcnt lgkmcnt(0)
	v_add_f32_e32 v20, v20, v22
	v_fmamk_f32 v20, v20, 0x3a000000, v31
	v_mul_f32_e32 v22, 0x4f800000, v20
	v_cmp_gt_f32_e32 vcc, s16, v20
	s_nop 1
	v_cndmask_b32_e32 v20, v20, v22, vcc
	v_sqrt_f32_e32 v22, v20
	s_nop 0
	v_add_u32_e32 v24, -1, v22
	v_add_u32_e32 v26, 1, v22
	v_fma_f32 v33, -v24, v22, v20
	v_fma_f32 v66, -v26, v22, v20
	v_cmp_ge_f32_e64 s[0:1], 0, v33
	s_nop 1
	v_cndmask_b32_e64 v22, v22, v24, s[0:1]
	v_cmp_lt_f32_e64 s[0:1], 0, v66
	s_nop 1
	v_cndmask_b32_e64 v22, v22, v26, s[0:1]
	v_mul_f32_e32 v24, 0x37800000, v22
	v_cndmask_b32_e32 v22, v22, v24, vcc
	v_cmp_class_f32_e32 vcc, v20, v32
	s_nop 1
	v_cndmask_b32_e32 v20, v22, v20, vcc
	v_div_scale_f32 v22, s[0:1], v20, v20, 1.0
	v_rcp_f32_e32 v26, v22
	v_div_scale_f32 v24, vcc, 1.0, v20, 1.0
	v_fma_f32 v33, -v22, v26, 1.0
	v_fmac_f32_e32 v26, v33, v26
	v_mul_f32_e32 v33, v24, v26
	v_fma_f32 v66, -v22, v33, v24
	v_fmac_f32_e32 v33, v66, v26
	v_fma_f32 v22, -v22, v33, v24
	v_div_fmas_f32 v22, v22, v26, v33
	v_div_fixup_f32 v20, v22, v20, 1.0
	v_pk_mul_f32 v[52:53], v[52:53], v[20:21] op_sel_hi:[1,0]
	v_pk_mul_f32 v[38:39], v[38:39], v[20:21] op_sel_hi:[1,0]
	v_pk_mul_f32 v[56:57], v[56:57], v[20:21] op_sel_hi:[1,0]
	v_pk_mul_f32 v[40:41], v[40:41], v[20:21] op_sel_hi:[1,0]
	v_pk_mul_f32 v[6:7], v[6:7], v[38:39]
	v_pk_mul_f32 v[4:5], v[4:5], v[52:53]
	v_pk_mul_f32 v[2:3], v[2:3], v[40:41]
	v_pk_mul_f32 v[0:1], v[0:1], v[56:57]
	global_store_dwordx4 v[18:19], v[4:7], off offset:-4096
	global_store_dwordx4 v[18:19], v[0:3], off offset:-4080
	s_nop 1
	v_mov_b32_e32 v0, v208
	v_mov_b32_e32 v1, v209
	v_mov_b32_e32 v2, v210
	v_mov_b32_e32 v3, v211
	s_nop 0
	v_mov_b32_e32 v4, v212
	v_mov_b32_e32 v5, v213
	v_mov_b32_e32 v6, v214
	v_mov_b32_e32 v7, v215
	v_pk_mul_f32 v[38:39], v[42:43], v[20:21] op_sel_hi:[1,0]
	v_pk_mul_f32 v[40:41], v[58:59], v[20:21] op_sel_hi:[1,0]
	v_pk_mul_f32 v[42:43], v[44:45], v[20:21] op_sel_hi:[1,0]
	v_pk_mul_f32 v[44:45], v[54:55], v[20:21] op_sel_hi:[1,0]
	v_pk_mul_f32 v[34:35], v[34:35], v[20:21] op_sel_hi:[1,0]
	v_pk_mul_f32 v[36:37], v[36:37], v[20:21] op_sel_hi:[1,0]
	s_nop 0
	v_pk_mul_f32 v[0:1], v[0:1], v[40:41]
	v_pk_mul_f32 v[2:3], v[2:3], v[38:39]
	s_nop 0
	v_pk_mul_f32 v[4:5], v[4:5], v[44:45]
	v_pk_mul_f32 v[6:7], v[6:7], v[42:43]
	global_store_dwordx4 v[18:19], v[0:3], off offset:-2048
	global_store_dwordx4 v[18:19], v[4:7], off offset:-2032
	s_nop 1
	v_mov_b32_e32 v0, v216
	v_mov_b32_e32 v1, v217
	v_mov_b32_e32 v2, v218
	v_mov_b32_e32 v3, v219
	s_nop 0
	v_mov_b32_e32 v4, v220
	v_mov_b32_e32 v5, v221
	v_mov_b32_e32 v6, v222
	v_mov_b32_e32 v7, v223
	v_pk_mul_f32 v[38:39], v[46:47], v[20:21] op_sel_hi:[1,0]
	v_pk_mul_f32 v[40:41], v[62:63], v[20:21] op_sel_hi:[1,0]
	v_pk_mul_f32 v[42:43], v[48:49], v[20:21] op_sel_hi:[1,0]
	v_pk_mul_f32 v[44:45], v[60:61], v[20:21] op_sel_hi:[1,0]
	s_nop 0
	v_pk_mul_f32 v[0:1], v[0:1], v[40:41]
	v_pk_mul_f32 v[2:3], v[2:3], v[38:39]
	s_nop 0
	v_pk_mul_f32 v[4:5], v[4:5], v[44:45]
	v_pk_mul_f32 v[6:7], v[6:7], v[42:43]
	global_store_dwordx4 v[18:19], v[0:3], off
	global_store_dwordx4 v[18:19], v[4:7], off offset:16
	s_nop 1
	v_mov_b32_e32 v0, v224
	v_mov_b32_e32 v1, v225
	v_mov_b32_e32 v2, v226
	v_mov_b32_e32 v3, v227
	s_nop 0
	v_mov_b32_e32 v4, v228
	v_mov_b32_e32 v5, v229
	v_mov_b32_e32 v6, v230
	v_mov_b32_e32 v7, v231
	v_pk_mul_f32 v[38:39], v[50:51], v[20:21] op_sel_hi:[1,0]
	v_pk_mul_f32 v[40:41], v[64:65], v[20:21] op_sel_hi:[1,0]
	s_nop 0
	v_pk_mul_f32 v[0:1], v[0:1], v[36:37]
	v_pk_mul_f32 v[2:3], v[2:3], v[34:35]
	s_nop 0
	v_pk_mul_f32 v[4:5], v[4:5], v[40:41]
	v_pk_mul_f32 v[6:7], v[6:7], v[38:39]
	global_store_dwordx4 v[18:19], v[0:3], off offset:2048
	global_store_dwordx4 v[18:19], v[4:7], off offset:2064
	v_lshl_add_u64 v[18:19], v[18:19], 0, s[6:7]
	s_cbranch_scc1 .LBB0_1506
